# lever 7.4: one static s_setprio 1 for waves 4-7 across the latent attention tile loop (reset at loop exit)
# baseline (speedup 1.0000x reference)
.LBB0_438:
	s_lshl_b32 s2, s12, 1
	s_and_b32 s2, s2, 14
	s_ashr_i32 s3, s12, 7
	s_add_i32 s2, s2, s3
	s_ashr_i32 s3, s2, 2
	s_lshl_b32 s22, s3, 8
	s_lshl_b32 s21, s3, 12
	s_lshl_b32 s3, s12, 5
	s_lshl_b32 s2, s2, 7
	v_mov_b32_e32 v205, v3
	v_readlane_b32 s8, v254, 27
	s_and_b32 s3, s3, 0xf00
	s_and_b32 s10, s2, 0x180
	v_mbcnt_lo_u32_b32 v0, -1, 0
	v_mbcnt_hi_u32_b32 v0, -1, v0
	s_add_i32 s13, s22, 0x4000
	v_add_u32_e32 v204, s8, v0
	s_or_b32 s11, s21, s3
	s_lshl_b32 s80, s10, 1
	s_add_u32 s2, s52, s80
	v_lshlrev_b32_e32 v0, 4, v204
	v_add_u32_e32 v6, 0x200, v204
	v_add_u32_e32 v12, 0x400, v204
	v_add_u32_e32 v14, 0x600, v204
	s_addc_u32 s3, s53, 0
	v_and_b32_e32 v2, 0xf0, v0
	v_ashrrev_i32_e32 v36, 4, v204
	v_ashrrev_i32_e32 v38, 4, v6
	v_ashrrev_i32_e32 v40, 4, v12
	v_ashrrev_i32_e32 v42, 4, v14
	v_add_u32_e32 v20, 0x800, v204
	v_add_u32_e32 v22, 0xa00, v204
	v_lshl_add_u64 v[0:1], s[2:3], 0, v[2:3]
	v_add_u32_e32 v4, s11, v36
	s_movk_i32 s18, 0x1400
	v_add_u32_e32 v6, s11, v38
	v_add_u32_e32 v12, s11, v40
	v_add_u32_e32 v14, s11, v42
	v_ashrrev_i32_e32 v44, 4, v20
	v_ashrrev_i32_e32 v46, 4, v22
	v_add_u32_e32 v28, 0xc00, v204
	v_add_u32_e32 v32, 0xe00, v204
	v_mad_i64_i32 v[4:5], s[8:9], v4, s18, v[0:1]
	v_mad_i64_i32 v[8:9], s[8:9], v6, s18, v[0:1]
	v_mad_i64_i32 v[12:13], s[8:9], v12, s18, v[0:1]
	v_mad_i64_i32 v[16:17], s[8:9], v14, s18, v[0:1]
	v_add_u32_e32 v20, s11, v44
	v_add_u32_e32 v22, s11, v46
	v_ashrrev_i32_e32 v47, 4, v28
	v_ashrrev_i32_e32 v48, 4, v32
	global_load_dwordx4 v[4:7], v[4:5], off
	s_nop 0
	global_load_dwordx4 v[8:11], v[8:9], off
	s_nop 0
	global_load_dwordx4 v[12:15], v[12:13], off
	s_nop 0
	global_load_dwordx4 v[16:19], v[16:17], off
	v_mad_i64_i32 v[20:21], s[8:9], v20, s18, v[0:1]
	v_mad_i64_i32 v[24:25], s[8:9], v22, s18, v[0:1]
	v_add_u32_e32 v28, s11, v47
	v_add_u32_e32 v32, s11, v48
	global_load_dwordx4 v[20:23], v[20:21], off
	s_nop 0
	global_load_dwordx4 v[24:27], v[24:25], off
	v_mad_i64_i32 v[28:29], s[8:9], v28, s18, v[0:1]
	v_mad_i64_i32 v[0:1], s[8:9], v32, s18, v[0:1]
	global_load_dwordx4 v[28:31], v[28:29], off
	v_add_u32_e32 v206, 0x11800, v205
	global_load_dwordx4 v[32:35], v[0:1], off
	v_add_u32_e32 v0, v206, v2
	v_mad_u64_u32 v[36:37], s[14:15], v36, s30, v[0:1]
	v_mad_u64_u32 v[38:39], s[14:15], v38, s30, v[0:1]
	v_mad_u64_u32 v[40:41], s[14:15], v40, s30, v[0:1]
	v_mad_u64_u32 v[42:43], s[14:15], v42, s30, v[0:1]
	v_mad_u64_u32 v[44:45], s[14:15], v44, s30, v[0:1]
	v_and_b32_e32 v2, 63, v204
	v_ashrrev_i32_e32 v49, 6, v204
	s_mov_b64 s[24:25], 0x400
	v_readfirstlane_b32 s8, v49
	s_mov_b32 s23, 0
	v_mov_b32_e32 v210, 0
	v_mov_b32_e32 v208, 0xf149f2ca
	v_mov_b32_e32 v209, 0xf149f2ca
	v_mov_b32_e32 v207, 0
	s_waitcnt vmcnt(7)
	ds_write_b128 v36, v[4:7]
	s_waitcnt vmcnt(6)
	ds_write_b128 v38, v[8:11]
	s_waitcnt vmcnt(5)
	ds_write_b128 v40, v[12:15]
	s_waitcnt vmcnt(4)
	ds_write_b128 v42, v[16:19]
	s_waitcnt vmcnt(3)
	ds_write_b128 v44, v[20:23]
	v_mad_u64_u32 v[4:5], s[14:15], v46, s30, v[0:1]
	s_waitcnt vmcnt(2)
	ds_write_b128 v4, v[24:27]
	v_mad_u64_u32 v[4:5], s[14:15], v47, s30, v[0:1]
	v_mad_u64_u32 v[0:1], s[14:15], v48, s30, v[0:1]
	s_waitcnt vmcnt(1)
	ds_write_b128 v4, v[28:31]
	s_waitcnt vmcnt(0)
	ds_write_b128 v0, v[32:35]
	v_or_b32_e32 v4, s13, v2
	v_mov_b64_e32 v[0:1], s[52:53]
	v_mad_i64_i32 v[0:1], s[14:15], v4, s18, v[0:1]
	s_lshl_b32 s14, s8, 3
	s_add_i32 s15, s21, 0xffffff00
	s_cmp_lt_i32 s8, 32
	s_cselect_b32 s9, s13, s15
	s_add_i32 s9, s9, s14
	s_mul_hi_i32 s18, s9, 0x1400
	s_mulk_i32 s9, 0x1400
	s_add_u32 s9, s52, s9
	v_lshlrev_b32_e32 v4, 3, v49
	s_addc_u32 s19, s53, s18
	v_lshl_add_u64 v[0:1], v[0:1], 0, s[80:81]
	v_ashrrev_i32_e32 v5, 31, v4
	s_add_u32 s18, s9, s80
	v_lshl_add_u64 v[0:1], v[4:5], 1, v[0:1]
	s_addc_u32 s19, s19, 0
	v_lshlrev_b32_e32 v2, 2, v2
	global_load_dwordx4 v[176:179], v[0:1], off offset:2048
	global_load_dwordx4 v[180:183], v[0:1], off offset:2176
	v_lshl_add_u64 v[0:1], s[18:19], 0, v[2:3]
	s_mul_i32 s19, s8, 0x880
	v_add_u32_e32 v4, s19, v205
	s_or_b32 s20, s14, 1
	v_readfirstlane_b32 s9, v4
	s_cmpk_lt_i32 s20, 0x100
	s_mov_b32 m0, s9
	s_cselect_b32 s9, s13, s15
	s_add_i32 s9, s9, s20
	s_mul_hi_i32 s18, s9, 0x1400
	s_mulk_i32 s9, 0x1400
	s_add_u32 s9, s52, s9
	s_mulk_i32 s20, 0x110
	s_addc_u32 s18, s53, s18
	v_add_u32_e32 v4, s20, v205
	v_lshl_add_u64 v[0:1], v[0:1], 0, s[24:25]
	s_add_u32 s26, s9, s80
	v_readfirstlane_b32 s9, v4
	global_load_lds_dword v[0:1], off
	s_addc_u32 s27, s18, 0
	s_mov_b32 m0, s9
	s_or_b32 s9, s14, 2
	s_cmpk_lt_i32 s9, 0x100
	s_cselect_b32 s18, s13, s15
	s_add_i32 s9, s18, s9
	s_mul_hi_i32 s18, s9, 0x1400
	s_mulk_i32 s9, 0x1400
	s_add_u32 s9, s52, s9
	s_addc_u32 s18, s53, s18
	v_lshl_add_u64 v[0:1], s[26:27], 0, v[2:3]
	s_add_u32 s26, s9, s80
	s_addc_u32 s27, s18, 0
	s_add_i32 s9, s20, 0x110
	v_add_u32_e32 v4, s9, v205
	v_lshl_add_u64 v[0:1], v[0:1], 0, s[24:25]
	v_readfirstlane_b32 s9, v4
	global_load_lds_dword v[0:1], off
	s_mov_b32 m0, s9
	s_or_b32 s9, s14, 3
	s_cmpk_lt_i32 s9, 0x100
	s_cselect_b32 s18, s13, s15
	s_add_i32 s9, s18, s9
	s_mul_hi_i32 s18, s9, 0x1400
	s_mulk_i32 s9, 0x1400
	s_add_u32 s9, s52, s9
	s_addc_u32 s18, s53, s18
	v_lshl_add_u64 v[0:1], s[26:27], 0, v[2:3]
	s_add_u32 s26, s9, s80
	s_addc_u32 s27, s18, 0
	s_add_i32 s9, s20, 0x220
	v_add_u32_e32 v4, s9, v205
	v_lshl_add_u64 v[0:1], v[0:1], 0, s[24:25]
	v_readfirstlane_b32 s9, v4
	global_load_lds_dword v[0:1], off
	s_mov_b32 m0, s9
	s_or_b32 s9, s14, 4
	s_cmpk_lt_i32 s9, 0x100
	s_cselect_b32 s18, s13, s15
	s_add_i32 s9, s18, s9
	s_mul_hi_i32 s18, s9, 0x1400
	s_mulk_i32 s9, 0x1400
	s_add_u32 s9, s52, s9
	s_addc_u32 s18, s53, s18
	v_lshl_add_u64 v[0:1], s[26:27], 0, v[2:3]
	s_add_u32 s26, s9, s80
	s_addc_u32 s27, s18, 0
	s_add_i32 s9, s20, 0x330
	v_add_u32_e32 v4, s9, v205
	v_lshl_add_u64 v[0:1], v[0:1], 0, s[24:25]
	v_readfirstlane_b32 s9, v4
	global_load_lds_dword v[0:1], off
	s_mov_b32 m0, s9
	s_or_b32 s9, s14, 5
	s_cmpk_lt_i32 s9, 0x100
	s_cselect_b32 s18, s13, s15
	s_add_i32 s9, s18, s9
	s_mul_hi_i32 s18, s9, 0x1400
	s_mulk_i32 s9, 0x1400
	s_add_u32 s9, s52, s9
	s_addc_u32 s18, s53, s18
	v_lshl_add_u64 v[0:1], s[26:27], 0, v[2:3]
	s_add_u32 s26, s9, s80
	s_addc_u32 s27, s18, 0
	s_add_i32 s9, s20, 0x440
	v_add_u32_e32 v4, s9, v205
	v_lshl_add_u64 v[0:1], v[0:1], 0, s[24:25]
	v_readfirstlane_b32 s9, v4
	global_load_lds_dword v[0:1], off
	s_mov_b32 m0, s9
	s_or_b32 s9, s14, 6
	s_cmpk_lt_i32 s9, 0x100
	s_cselect_b32 s18, s13, s15
	s_add_i32 s9, s18, s9
	s_mul_hi_i32 s18, s9, 0x1400
	s_mulk_i32 s9, 0x1400
	s_add_u32 s9, s52, s9
	s_addc_u32 s18, s53, s18
	v_lshl_add_u64 v[0:1], s[26:27], 0, v[2:3]
	s_add_u32 s26, s9, s80
	s_addc_u32 s27, s18, 0
	s_add_i32 s9, s20, 0x550
	v_add_u32_e32 v4, s9, v205
	v_lshl_add_u64 v[0:1], v[0:1], 0, s[24:25]
	v_readfirstlane_b32 s9, v4
	global_load_lds_dword v[0:1], off
	s_mov_b32 m0, s9
	s_or_b32 s9, s14, 7
	s_cmpk_lt_i32 s9, 0x100
	s_cselect_b32 s18, s13, s15
	s_add_i32 s9, s18, s9
	s_mul_hi_i32 s18, s9, 0x1400
	s_mulk_i32 s9, 0x1400
	s_add_u32 s9, s52, s9
	s_addc_u32 s18, s53, s18
	v_lshl_add_u64 v[0:1], s[26:27], 0, v[2:3]
	s_add_u32 s26, s9, s80
	v_lshl_add_u64 v[0:1], v[0:1], 0, s[24:25]
	s_addc_u32 s27, s18, 0
	s_add_i32 s9, s20, 0x660
	global_load_lds_dword v[0:1], off
	v_lshl_add_u64 v[0:1], s[26:27], 0, v[2:3]
	v_add_u32_e32 v2, s9, v205
	v_lshl_add_u64 v[0:1], v[0:1], 0, s[24:25]
	v_readfirstlane_b32 s9, v2
	s_mov_b32 m0, s9
	s_movk_i32 s9, 0x480
	global_load_lds_dword v[0:1], off
	v_bfe_u32 v0, v204, 2, 2
	v_and_b32_e32 v1, 12, v204
	v_cmp_ne_u32_e32 vcc, 2, v0
	v_mov_b32_e32 v14, v3
	v_mov_b32_e32 v15, v3
	v_cndmask_b32_e32 v1, 4, v1, vcc
	v_cmp_ne_u32_e32 vcc, 1, v0
	v_mov_b32_e32 v2, v3
	v_mov_b32_e32 v4, v3
	v_cndmask_b32_e32 v0, 8, v1, vcc
	v_and_or_b32 v0, v204, 51, v0
	v_mul_lo_u32 v1, v49, s9
	v_lshlrev_b32_e32 v0, 1, v0
	v_add3_u32 v0, v205, v1, v0
	s_waitcnt vmcnt(0)
	ds_write_b16 v0, v176 offset:34816
	ds_write_b16_d16_hi v0, v176 offset:34960
	ds_write_b16 v0, v177 offset:35104
	ds_write_b16_d16_hi v0, v177 offset:35248
	ds_write_b16 v0, v178 offset:35392
	ds_write_b16_d16_hi v0, v178 offset:35536
	ds_write_b16 v0, v179 offset:35680
	ds_write_b16_d16_hi v0, v179 offset:35824
	ds_write_b16 v0, v180 offset:44032
	ds_write_b16_d16_hi v0, v180 offset:44176
	ds_write_b16 v0, v181 offset:44320
	ds_write_b16_d16_hi v0, v181 offset:44464
	ds_write_b16 v0, v182 offset:44608
	ds_write_b16_d16_hi v0, v182 offset:44752
	ds_write_b16 v0, v183 offset:44896
	ds_write_b16_d16_hi v0, v183 offset:45040
	v_mov_b32_e32 v0, v3
	v_mov_b32_e32 v1, v3
	v_mov_b32_e32 v5, v3
	v_mov_b32_e32 v6, v3
	v_mov_b32_e32 v7, v3
	v_mov_b32_e32 v8, v3
	v_mov_b32_e32 v9, v3
	v_mov_b32_e32 v10, v3
	v_mov_b32_e32 v11, v3
	v_mov_b32_e32 v12, v3
	v_mov_b32_e32 v13, v3
	v_mov_b64_e32 v[30:31], v[14:15]
	v_mov_b64_e32 v[62:63], v[14:15]
	v_mov_b64_e32 v[94:95], v[14:15]
	v_mov_b64_e32 v[126:127], v[14:15]
	v_mov_b64_e32 v[46:47], v[14:15]
	v_mov_b64_e32 v[78:79], v[14:15]
	v_mov_b64_e32 v[110:111], v[14:15]
	v_mov_b64_e32 v[142:143], v[14:15]
	s_lshl_b32 s18, s8, 5
	s_addk_i32 s21, 0xff40
	s_addk_i32 s22, 0x4040
	v_mov_b64_e32 v[28:29], v[12:13]
	v_mov_b64_e32 v[26:27], v[10:11]
	v_mov_b64_e32 v[24:25], v[8:9]
	v_mov_b64_e32 v[22:23], v[6:7]
	v_mov_b64_e32 v[20:21], v[4:5]
	v_mov_b64_e32 v[18:19], v[2:3]
	v_mov_b64_e32 v[16:17], v[0:1]
	v_mov_b64_e32 v[60:61], v[12:13]
	v_mov_b64_e32 v[58:59], v[10:11]
	v_mov_b64_e32 v[56:57], v[8:9]
	v_mov_b64_e32 v[54:55], v[6:7]
	v_mov_b64_e32 v[52:53], v[4:5]
	v_mov_b64_e32 v[50:51], v[2:3]
	v_mov_b64_e32 v[48:49], v[0:1]
	v_mov_b64_e32 v[92:93], v[12:13]
	v_mov_b64_e32 v[90:91], v[10:11]
	v_mov_b64_e32 v[88:89], v[8:9]
	v_mov_b64_e32 v[86:87], v[6:7]
	v_mov_b64_e32 v[84:85], v[4:5]
	v_mov_b64_e32 v[82:83], v[2:3]
	v_mov_b64_e32 v[80:81], v[0:1]
	v_mov_b64_e32 v[124:125], v[12:13]
	v_mov_b64_e32 v[122:123], v[10:11]
	v_mov_b64_e32 v[120:121], v[8:9]
	v_mov_b64_e32 v[118:119], v[6:7]
	v_mov_b64_e32 v[116:117], v[4:5]
	v_mov_b64_e32 v[114:115], v[2:3]
	v_mov_b64_e32 v[112:113], v[0:1]
	v_mov_b64_e32 v[44:45], v[12:13]
	v_mov_b64_e32 v[42:43], v[10:11]
	v_mov_b64_e32 v[40:41], v[8:9]
	v_mov_b64_e32 v[38:39], v[6:7]
	v_mov_b64_e32 v[36:37], v[4:5]
	v_mov_b64_e32 v[34:35], v[2:3]
	v_mov_b64_e32 v[32:33], v[0:1]
	v_mov_b64_e32 v[76:77], v[12:13]
	v_mov_b64_e32 v[74:75], v[10:11]
	v_mov_b64_e32 v[72:73], v[8:9]
	v_mov_b64_e32 v[70:71], v[6:7]
	v_mov_b64_e32 v[68:69], v[4:5]
	v_mov_b64_e32 v[66:67], v[2:3]
	v_mov_b64_e32 v[64:65], v[0:1]
	v_mov_b64_e32 v[108:109], v[12:13]
	v_mov_b64_e32 v[106:107], v[10:11]
	v_mov_b64_e32 v[104:105], v[8:9]
	v_mov_b64_e32 v[102:103], v[6:7]
	v_mov_b64_e32 v[100:101], v[4:5]
	v_mov_b64_e32 v[98:99], v[2:3]
	v_mov_b64_e32 v[96:97], v[0:1]
	v_mov_b64_e32 v[140:141], v[12:13]
	v_mov_b64_e32 v[138:139], v[10:11]
	v_mov_b64_e32 v[136:137], v[8:9]
	v_mov_b64_e32 v[134:135], v[6:7]
	v_mov_b64_e32 v[132:133], v[4:5]
	v_mov_b64_e32 v[130:131], v[2:3]
	v_mov_b64_e32 v[128:129], v[0:1]
	s_mov_b32 s26, 0
	s_waitcnt lgkmcnt(0)
	s_barrier
	v_and_b32_e32 v2, 31, v204
	v_bfe_u32 v15, v204, 5, 1
	v_lshlrev_b32_e32 v15, 4, v15
	v_or_b32_e32 v13, s18, v2
	v_mul_u32_u24_e32 v1, 0x90, v2
	v_mad_u32_u24 v0, v2, s30, v15
	v_mul_lo_u32 v13, v13, s30
	v_add_u32_e32 v0, v0, v205
	v_add3_u32 v1, v1, v15, v205
	v_add3_u32 v13, v206, v13, v15
	v_bfe_u32 v15, v204, 2, 2
	v_and_b32_e32 v2, 12, v204
	v_cmp_ne_u32_e32 vcc, 2, v15
	s_movk_i32 s8, 0x480
	v_ashrrev_i32_e32 v211, 6, v204
	v_cndmask_b32_e32 v2, 4, v2, vcc
	v_cmp_ne_u32_e32 vcc, 1, v15
	v_mul_lo_u32 v211, v211, s8
	s_nop 0
	v_cndmask_b32_e32 v15, 8, v2, vcc
	v_and_or_b32 v2, v204, 51, v15
	v_lshlrev_b32_e32 v2, 1, v2
	v_add3_u32 v2, v205, v211, v2
	s_lshr_b32 s8, s18, 5
	s_cmp_ge_u32 s8, 4
	s_cbranch_scc0 .Lmy_prio_a
	s_setprio 1
.Lmy_prio_a:
.LBB0_439:
	s_add_i32 s25, s26, 1
	s_and_b32 s27, s26, 1
	s_mul_i32 s24, s27, 0x4400
	s_mul_i32 s31, s27, 0x4800
	v_add_u32_e32 v12, s24, v0
	v_add_u32_e32 v14, s31, v1
	ds_read_b128 v[228:231], v12 offset:0
	ds_read_b128 v[232:235], v12 offset:32
	ds_read_b128 v[236:239], v12 offset:64
	ds_read_b128 v[240:243], v12 offset:96
	ds_read_b128 v[244:247], v13 offset:0
	ds_read_b128 v[248:251], v13 offset:32
	ds_read_b128 v[4:7], v13 offset:64
	ds_read_b128 v[8:11], v13 offset:96
	ds_read_b128 v[184:187], v14 offset:34816
	ds_read_b128 v[188:191], v14 offset:39424
	ds_read_b128 v[192:195], v14 offset:44032
	ds_read_b128 v[196:199], v14 offset:48640
	ds_read_b128 v[200:203], v14 offset:34848
	ds_read_b128 v[212:215], v14 offset:39456
	ds_read_b128 v[216:219], v14 offset:44064
	s_cmpk_gt_u32 s26, 0x42
	s_cbranch_scc1 .Lat_noload
	s_cmp_lt_u32 s26, 3
	s_cselect_b32 s24, s22, s21
	s_cselect_b32 s31, s13, s15
	s_add_i32 s24, s24, s23
	v_and_b32_e32 v15, 63, v204
	v_ashrrev_i32_e32 v227, 6, v204
	v_add_u32_e32 v211, s24, v15
	v_lshlrev_b32_e32 v227, 4, v227
	s_add_i32 s31, s31, s14
	v_mul_u32_u24_e32 v211, 0x1400, v211
	s_add_i32 s31, s31, s23
	s_add_i32 s31, s31, 64
	v_add_u32_e32 v211, v211, v227
	s_mul_hi_i32 s37, s31, 0x1400
	s_mul_i32 s36, s31, 0x1400
	v_lshlrev_b32_e32 v15, 2, v15
	global_load_dwordx4 v[176:179], v211, s[2:3] offset:2048
	global_load_dwordx4 v[180:183], v211, s[2:3] offset:2176
	s_add_u32 s36, s2, s36
	s_addc_u32 s37, s3, s37
	v_readfirstlane_b32 s38, v205
	s_xor_b32 s39, s27, 1
	v_add_u32_e32 v15, 0x400, v15
	s_mul_i32 s39, s39, 0x4400
	s_add_i32 s38, s38, s19
	s_add_i32 s38, s38, s39
	s_add_i32 m0, s38, 0
	s_nop 0
	global_load_lds_dword v15, s[36:37]
	s_add_u32 s36, s36, 0x1400
	s_addc_u32 s37, s37, 0
	s_add_i32 m0, s38, 272
	s_nop 0
	global_load_lds_dword v15, s[36:37]
	s_add_u32 s36, s36, 0x1400
	s_addc_u32 s37, s37, 0
	s_add_i32 m0, s38, 544
	s_nop 0
	global_load_lds_dword v15, s[36:37]
	s_add_u32 s36, s36, 0x1400
	s_addc_u32 s37, s37, 0
	s_add_i32 m0, s38, 816
	s_nop 0
	global_load_lds_dword v15, s[36:37]
	s_add_u32 s36, s36, 0x1400
	s_addc_u32 s37, s37, 0
	s_add_i32 m0, s38, 1088
	s_nop 0
	global_load_lds_dword v15, s[36:37]
	s_add_u32 s36, s36, 0x1400
	s_addc_u32 s37, s37, 0
	s_add_i32 m0, s38, 1360
	s_nop 0
	global_load_lds_dword v15, s[36:37]
	s_add_u32 s36, s36, 0x1400
	s_addc_u32 s37, s37, 0
	s_add_i32 m0, s38, 1632
	s_nop 0
	global_load_lds_dword v15, s[36:37]
	s_add_u32 s36, s36, 0x1400
	s_addc_u32 s37, s37, 0
	s_add_i32 m0, s38, 1904
	s_nop 0
	global_load_lds_dword v15, s[36:37]

.Lat_exit:
	s_setprio 0
	s_mov_b32 s26, s27
	s_nop 15
	s_branch .LBB0_437
